# stack + NSA static prio for waves 4-7 + counted wait in W_in-side conversion
# speedup vs baseline: 1.0021x; 1.0021x over previous
; __device__ __forceinline__ unsigned cvt_pk_bf16(float lo, float hi) { f32x2_t v = {lo, hi}; bf16x2_t b = __builtin_convertvector(v, bf16x2_t); return __builtin_bit_cast(unsigned, b); }
; __device__ __forceinline__ void conv_span128(const float* W, int ldw, int K, bf16* WT, int rowmode, int kb, int n0, int lane) {
;     const int c = lane & 7, nn = lane >> 3;
;     const float* src = W + (size_t)(kb * 64 + 8 * c) * ldw + n0 + 4 * nn;
;     f32x4 v[4][8];
; #pragma unroll
;     for (int h = 0; h < 4; ++h)
; #pragma unroll
;         for (int i = 0; i < 8; ++i) v[h][i] = __builtin_nontemporal_load((const f32x4*)(src + 32 * h + (size_t)i * ldw));
; #pragma unroll
;     for (int h = 0; h < 4; ++h) {
;         const int n = n0 + 32 * h + 4 * nn; int r = n;
;         if (rowmode == 2) r = ((n >> 7) << 8) + (n & 127);
;         else if (rowmode == 3) r = ((n >> 7) << 8) + 128 + (n & 127);
;         bf16* d0 = WT + (size_t)r * K + kb * 64 + 8 * c;
; #pragma unroll
;         for (int j = 0; j < 4; ++j) { u32x4 o; o.x = cvt_pk_bf16(v[h][0][j], v[h][1][j]); o.y = cvt_pk_bf16(v[h][2][j], v[h][3][j]); o.z = cvt_pk_bf16(v[h][4][j], v[h][5][j]); o.w = cvt_pk_bf16(v[h][6][j], v[h][7][j]);
;             *(u32x4*)(d0 + (size_t)j * K) = o; }
;     }
;     ...
;         const int p = (int)(cur & 0x7FFFFFFFu);
;         if ((cur >> 31) == 0u) { const int e = p / 448, w3 = (p / 224) & 1, q = p % 224;
;             conv_span128((w3 ? m3 : m1) + (size_t)e * D * FFE, FFE, D, mup + (size_t)e * 2 * FFE * D, 2 + w3, q / 7, (q % 7) * 1024 + wave * 128, lane); }
;         else { const int e = p / 224, q = p % 224, kb = q >> 1, h = kb / 56;
;             conv_span128(m2 + (size_t)e * FFE * D + (size_t)h * (FFE / 2) * D, 2048, FFE / 2, mdn + (size_t)(e * 2 + h) * D * (FFE / 2), 0, kb - 56 * h, (q & 1) * 1024 + wave * 128, lane); }
.LBB0_151:
	s_or_b64 exec, exec, s[6:7]
	s_and_b32 s8, s20, 0x7fffffff
	s_cmp_lt_i32 s20, 0
	s_mov_b64 s[6:7], -1
	s_cbranch_scc0 .LBB0_153
	s_lshr_b32 s6, s8, 5
	s_mul_hi_u32 s9, s6, 0x24924925
	s_mul_i32 s6, s9, 0xe0
	s_sub_i32 s12, s8, s6
	s_lshr_b32 s13, s12, 1
	s_cmpk_gt_u32 s12, 0x6f
	s_mul_i32 s11, s9, 0x3800000
	v_readlane_b32 s40, v255, 3
	s_cselect_b64 s[6:7], -1, 0
	s_mul_hi_u32 s10, s9, 0x3800000
	v_readlane_b32 s41, v255, 4
	s_add_u32 s14, s40, s11
	s_addc_u32 s15, s41, s10
	s_and_b64 s[10:11], s[6:7], exec
	s_cselect_b32 s10, 0x1c00000, 0
	v_cndmask_b32_e64 v2, 0, 1, s[6:7]
	s_add_u32 s10, s14, s10
	s_addc_u32 s11, s15, 0
	s_lshl_b32 s9, s9, 1
	v_readfirstlane_b32 s14, v2
	s_or_b32 s9, s9, s14
	s_mul_hi_u32 s14, s9, 0xe00000
	s_mul_i32 s9, s9, 0xe00000
	v_readlane_b32 s15, v250, 16
	s_add_u32 s9, s15, s9
	v_readlane_b32 s15, v250, 17
	s_addc_u32 s14, s15, s14
	s_and_b64 s[6:7], s[6:7], exec
	s_cselect_b32 s6, 0xffffffc8, 0
	s_add_i32 s7, s6, s13
	s_lshl_b32 s6, s12, 10
	s_lshl_b32 s12, s7, 6
	v_or_b32_e32 v2, s12, v126
	s_and_b32 s6, s6, 0x400
	v_ashrrev_i32_e32 v3, 31, v2
	s_add_i32 s6, s6, s18
	v_lshlrev_b64 v[2:3], 13, v[2:3]
	v_lshl_add_u64 v[2:3], s[10:11], 0, v[2:3]
	s_ashr_i32 s7, s6, 31
	v_lshl_add_u64 v[2:3], s[6:7], 2, v[2:3]
	v_mov_b32_e32 v131, v187
	v_lshl_add_u64 v[2:3], v[2:3], 0, v[130:131]
	s_movk_i32 s7, 0x2000
	v_add_co_u32_e32 v6, vcc, s7, v2
	s_movk_i32 s7, 0x4000
	s_nop 0
	v_addc_co_u32_e32 v7, vcc, 0, v3, vcc
	v_add_co_u32_e32 v10, vcc, s7, v2
	s_movk_i32 s7, 0x6000
	s_nop 0
	v_addc_co_u32_e32 v11, vcc, 0, v3, vcc
	v_add_co_u32_e32 v14, vcc, s7, v2
	s_mov_b32 s7, 0x8000
	s_nop 0
	v_addc_co_u32_e32 v15, vcc, 0, v3, vcc
	v_add_co_u32_e32 v18, vcc, s7, v2
	s_mov_b32 s7, 0xa000
	s_nop 0
	v_addc_co_u32_e32 v19, vcc, 0, v3, vcc
	v_add_co_u32_e32 v22, vcc, s7, v2
	s_mov_b32 s7, 0xc000
	s_nop 0
	v_addc_co_u32_e32 v23, vcc, 0, v3, vcc
	v_add_co_u32_e32 v26, vcc, s7, v2
	global_load_dwordx4 v[98:101], v[2:3], off nt
	global_load_dwordx4 v[102:105], v[6:7], off nt
	v_addc_co_u32_e32 v27, vcc, 0, v3, vcc
	global_load_dwordx4 v[106:109], v[10:11], off nt
	global_load_dwordx4 v[110:113], v[14:15], off nt
	global_load_dwordx4 v[114:117], v[18:19], off nt
	global_load_dwordx4 v[118:121], v[22:23], off nt
	global_load_dwordx4 v[122:125], v[26:27], off nt
	s_mov_b32 s7, 0xe000
	v_add_co_u32_e32 v30, vcc, s7, v2
	s_ashr_i32 s13, s12, 31
	s_nop 0
	v_addc_co_u32_e32 v31, vcc, 0, v3, vcc
	global_load_dwordx4 v[134:137], v[30:31], off nt
	global_load_dwordx4 v[66:69], v[2:3], off offset:128 nt
	global_load_dwordx4 v[70:73], v[6:7], off offset:128 nt
	global_load_dwordx4 v[74:77], v[10:11], off offset:128 nt
	global_load_dwordx4 v[78:81], v[14:15], off offset:128 nt
	global_load_dwordx4 v[82:85], v[18:19], off offset:128 nt
	global_load_dwordx4 v[86:89], v[22:23], off offset:128 nt
	global_load_dwordx4 v[90:93], v[26:27], off offset:128 nt
	global_load_dwordx4 v[94:97], v[30:31], off offset:128 nt
	global_load_dwordx4 v[34:37], v[2:3], off offset:256 nt
	global_load_dwordx4 v[38:41], v[6:7], off offset:256 nt
	global_load_dwordx4 v[42:45], v[10:11], off offset:256 nt
	global_load_dwordx4 v[46:49], v[14:15], off offset:256 nt
	global_load_dwordx4 v[50:53], v[18:19], off offset:256 nt
	global_load_dwordx4 v[54:57], v[22:23], off offset:256 nt
	global_load_dwordx4 v[58:61], v[26:27], off offset:256 nt
	global_load_dwordx4 v[62:65], v[30:31], off offset:256 nt
	s_nop 0
	global_load_dwordx4 v[2:5], v[2:3], off offset:384 nt
	s_nop 0
	global_load_dwordx4 v[6:9], v[6:7], off offset:384 nt
	s_nop 0
	global_load_dwordx4 v[10:13], v[10:11], off offset:384 nt
	s_nop 0
	global_load_dwordx4 v[14:17], v[14:15], off offset:384 nt
	s_nop 0
	global_load_dwordx4 v[18:21], v[18:19], off offset:384 nt
	s_nop 0
	global_load_dwordx4 v[22:25], v[22:23], off offset:384 nt
	s_nop 0
	global_load_dwordx4 v[26:29], v[26:27], off offset:384 nt
	s_nop 0
	global_load_dwordx4 v[30:33], v[30:31], off offset:384 nt
	v_or_b32_e32 v131, s6, v128
	s_lshl_b64 s[6:7], s[12:13], 1
	s_add_u32 s6, s9, s6
	s_addc_u32 s7, s14, s7
	v_mov_b32_e32 v133, v187
	v_lshl_add_u64 v[142:143], s[6:7], 0, v[132:133]
	s_movk_i32 s10, 0x1c00
	v_mad_i64_i32 v[144:145], s[6:7], v131, s10, v[142:143]
	s_movk_i32 s9, 0x1000
	s_movk_i32 s11, 0x3000
	s_movk_i32 s12, 0x5000
	v_readlane_b32 s42, v255, 5
	v_readlane_b32 s43, v255, 6
	s_movk_i32 s97, 0x1000
	s_waitcnt vmcnt(30)
	v_cvt_pk_bf16_f32 v138, v98, v102
	v_add_co_u32_e32 v98, vcc, s9, v144
	s_waitcnt vmcnt(28)
	v_cvt_pk_bf16_f32 v139, v106, v110
	s_waitcnt vmcnt(26)
	v_cvt_pk_bf16_f32 v140, v114, v118
	s_waitcnt vmcnt(24)
	v_cvt_pk_bf16_f32 v141, v122, v134
	global_store_dwordx4 v[144:145], v[138:141], off
	s_nop 1
	v_cvt_pk_bf16_f32 v138, v99, v103
	v_cvt_pk_bf16_f32 v139, v107, v111
	v_cvt_pk_bf16_f32 v140, v115, v119
	v_cvt_pk_bf16_f32 v141, v123, v135
	v_addc_co_u32_e32 v99, vcc, 0, v145, vcc
	global_store_dwordx4 v[98:99], v[138:141], off offset:3072
	v_add_co_u32_e32 v98, vcc, s11, v144
	s_nop 0
	v_cvt_pk_bf16_f32 v138, v100, v104
	v_addc_co_u32_e32 v99, vcc, 0, v145, vcc
	v_cvt_pk_bf16_f32 v139, v108, v112
	v_cvt_pk_bf16_f32 v140, v116, v120
	v_cvt_pk_bf16_f32 v141, v124, v136
	v_add_co_u32_e32 v102, vcc, s12, v144
	global_store_dwordx4 v[98:99], v[138:141], off offset:2048
	v_cvt_pk_bf16_f32 v98, v101, v105
	v_cvt_pk_bf16_f32 v99, v109, v113
	v_cvt_pk_bf16_f32 v100, v117, v121
	v_cvt_pk_bf16_f32 v101, v125, v137
	v_addc_co_u32_e32 v103, vcc, 0, v145, vcc
	global_store_dwordx4 v[102:103], v[98:101], off offset:1024
	s_nop 1
	v_or_b32_e32 v98, 32, v131
	v_mad_i64_i32 v[102:103], s[6:7], v98, s10, v[142:143]
	s_waitcnt vmcnt(26)
; __device__ __forceinline__ unsigned cvt_pk_bf16(float lo, float hi) { f32x2_t v = {lo, hi}; bf16x2_t b = __builtin_convertvector(v, bf16x2_t); return __builtin_bit_cast(unsigned, b); }
; __device__ __forceinline__ void conv_span128(const float* W, int ldw, int K, bf16* WT, int rowmode, int kb, int n0, int lane) {
;     const int c = lane & 7, nn = lane >> 3;
;     const float* src = W + (size_t)(kb * 64 + 8 * c) * ldw + n0 + 4 * nn;
;     f32x4 v[4][8];
; #pragma unroll
;     for (int h = 0; h < 4; ++h)
; #pragma unroll
;         for (int i = 0; i < 8; ++i) v[h][i] = __builtin_nontemporal_load((const f32x4*)(src + 32 * h + (size_t)i * ldw));
; #pragma unroll
;     for (int h = 0; h < 4; ++h) {
;         const int n = n0 + 32 * h + 4 * nn; int r = n;
;         if (rowmode == 2) r = ((n >> 7) << 8) + (n & 127);
;         else if (rowmode == 3) r = ((n >> 7) << 8) + 128 + (n & 127);
;         bf16* d0 = WT + (size_t)r * K + kb * 64 + 8 * c;
; #pragma unroll
;         for (int j = 0; j < 4; ++j) { u32x4 o; o.x = cvt_pk_bf16(v[h][0][j], v[h][1][j]); o.y = cvt_pk_bf16(v[h][2][j], v[h][3][j]); o.z = cvt_pk_bf16(v[h][4][j], v[h][5][j]); o.w = cvt_pk_bf16(v[h][6][j], v[h][7][j]);
;             *(u32x4*)(d0 + (size_t)j * K) = o; }
;     }
;     ...
;         const int p = (int)(cur & 0x7FFFFFFFu);
;         if ((cur >> 31) == 0u) { const int e = p / 448, w3 = (p / 224) & 1, q = p % 224;
;             conv_span128((w3 ? m3 : m1) + (size_t)e * D * FFE, FFE, D, mup + (size_t)e * 2 * FFE * D, 2 + w3, q / 7, (q % 7) * 1024 + wave * 128, lane); }
	v_cvt_pk_bf16_f32 v98, v66, v70
	s_waitcnt vmcnt(24)
	v_cvt_pk_bf16_f32 v99, v74, v78
	s_waitcnt vmcnt(22)
	v_cvt_pk_bf16_f32 v100, v82, v86
	s_waitcnt vmcnt(20)
	v_cvt_pk_bf16_f32 v101, v90, v94
	v_add_co_u32_e32 v66, vcc, s9, v102
	global_store_dwordx4 v[102:103], v[98:101], off
	s_nop 1
	v_cvt_pk_bf16_f32 v98, v67, v71
	v_cvt_pk_bf16_f32 v99, v75, v79
	v_cvt_pk_bf16_f32 v100, v83, v87
	v_cvt_pk_bf16_f32 v101, v91, v95
	v_addc_co_u32_e32 v67, vcc, 0, v103, vcc
	global_store_dwordx4 v[66:67], v[98:101], off offset:3072
	v_add_co_u32_e32 v66, vcc, s11, v102
	s_nop 0
	v_cvt_pk_bf16_f32 v98, v68, v72
	v_addc_co_u32_e32 v67, vcc, 0, v103, vcc
	v_cvt_pk_bf16_f32 v99, v76, v80
	v_cvt_pk_bf16_f32 v100, v84, v88
	v_cvt_pk_bf16_f32 v101, v92, v96
	v_add_co_u32_e32 v70, vcc, s12, v102
	global_store_dwordx4 v[66:67], v[98:101], off offset:2048
	v_cvt_pk_bf16_f32 v66, v69, v73
	v_cvt_pk_bf16_f32 v67, v77, v81
	v_cvt_pk_bf16_f32 v68, v85, v89
	v_cvt_pk_bf16_f32 v69, v93, v97
	v_addc_co_u32_e32 v71, vcc, 0, v103, vcc
	global_store_dwordx4 v[70:71], v[66:69], off offset:1024
	s_nop 1
	v_or_b32_e32 v66, 64, v131
	v_mad_i64_i32 v[70:71], s[6:7], v66, s10, v[142:143]
	s_waitcnt vmcnt(22)
	v_cvt_pk_bf16_f32 v66, v34, v38
	s_waitcnt vmcnt(20)
	v_cvt_pk_bf16_f32 v67, v42, v46
	s_waitcnt vmcnt(18)
	v_cvt_pk_bf16_f32 v68, v50, v54
	s_waitcnt vmcnt(16)
	v_cvt_pk_bf16_f32 v69, v58, v62
	v_add_co_u32_e32 v34, vcc, s9, v70
	global_store_dwordx4 v[70:71], v[66:69], off
	s_nop 1
	v_cvt_pk_bf16_f32 v66, v35, v39
	v_cvt_pk_bf16_f32 v67, v43, v47
	v_cvt_pk_bf16_f32 v68, v51, v55
	v_cvt_pk_bf16_f32 v69, v59, v63
	v_addc_co_u32_e32 v35, vcc, 0, v71, vcc
	global_store_dwordx4 v[34:35], v[66:69], off offset:3072
	v_add_co_u32_e32 v34, vcc, s11, v70
	s_nop 0
	v_cvt_pk_bf16_f32 v66, v36, v40
	v_addc_co_u32_e32 v35, vcc, 0, v71, vcc
	v_cvt_pk_bf16_f32 v67, v44, v48
	v_cvt_pk_bf16_f32 v68, v52, v56
	v_cvt_pk_bf16_f32 v69, v60, v64
	v_add_co_u32_e32 v38, vcc, s12, v70
	global_store_dwordx4 v[34:35], v[66:69], off offset:2048
	v_cvt_pk_bf16_f32 v34, v37, v41
	v_cvt_pk_bf16_f32 v35, v45, v49
	v_cvt_pk_bf16_f32 v36, v53, v57
	v_cvt_pk_bf16_f32 v37, v61, v65
	v_addc_co_u32_e32 v39, vcc, 0, v71, vcc
	global_store_dwordx4 v[38:39], v[34:37], off offset:1024
	s_nop 1
	v_or_b32_e32 v34, 0x60, v131
	v_mad_i64_i32 v[38:39], s[6:7], v34, s10, v[142:143]
	s_waitcnt vmcnt(18)
	v_cvt_pk_bf16_f32 v34, v2, v6
	s_waitcnt vmcnt(16)
	v_cvt_pk_bf16_f32 v35, v10, v14
	s_waitcnt vmcnt(14)
	v_cvt_pk_bf16_f32 v36, v18, v22
	s_waitcnt vmcnt(12)
	v_cvt_pk_bf16_f32 v37, v26, v30
	v_add_co_u32_e32 v2, vcc, s9, v38
	global_store_dwordx4 v[38:39], v[34:37], off
	s_mov_b64 s[6:7], 0
	s_nop 0
	v_cvt_pk_bf16_f32 v34, v3, v7
	v_cvt_pk_bf16_f32 v35, v11, v15
	v_cvt_pk_bf16_f32 v36, v19, v23
	v_cvt_pk_bf16_f32 v37, v27, v31
	v_addc_co_u32_e32 v3, vcc, 0, v39, vcc
	global_store_dwordx4 v[2:3], v[34:37], off offset:3072
	v_add_co_u32_e32 v2, vcc, s11, v38
	s_nop 0
	v_cvt_pk_bf16_f32 v34, v4, v8
	v_addc_co_u32_e32 v3, vcc, 0, v39, vcc
	v_cvt_pk_bf16_f32 v35, v12, v16
	v_cvt_pk_bf16_f32 v36, v20, v24
	v_cvt_pk_bf16_f32 v37, v28, v32
	v_add_co_u32_e32 v6, vcc, 0x5000, v38
	global_store_dwordx4 v[2:3], v[34:37], off offset:2048
	v_cvt_pk_bf16_f32 v2, v5, v9
	v_cvt_pk_bf16_f32 v3, v13, v17
	v_cvt_pk_bf16_f32 v4, v21, v25
	v_cvt_pk_bf16_f32 v5, v29, v33
	v_addc_co_u32_e32 v7, vcc, 0, v39, vcc
	global_store_dwordx4 v[6:7], v[2:5], off offset:1024
.LBB0_153:
	s_andn2_b64 vcc, exec, s[6:7]
	s_cbranch_vccnz .LBB0_135
	s_lshr_b32 s7, s20, 5
	s_mul_hi_u32 s7, s7, 0x24924925
	s_and_b32 s12, s7, 1
	s_mul_hi_u32 s7, s8, 0x92492493
	s_lshr_b32 s7, s7, 7
	s_mulk_i32 s7, 0xe0
	s_lshr_b32 s6, s20, 6
	s_sub_i32 s10, s8, s7
	v_readlane_b32 s40, v255, 7
	s_mul_hi_u32 s6, s6, 0x24924925
	s_cmp_eq_u32 s12, 0
	v_readlane_b32 s44, v255, 11
	v_readlane_b32 s46, v255, 13
	v_readlane_b32 s45, v255, 12
	v_readlane_b32 s47, v255, 14
	s_cselect_b32 s8, s44, s46
	s_mul_hi_u32 s11, s6, 0x3800000
	s_mul_i32 s13, s6, 0x3800000
	s_movk_i32 s6, 0x60
	s_cselect_b32 s9, s45, s47
	s_cselect_b32 s14, 32, 0xa0
	s_cselect_b32 s7, 64, 0xc0
	s_cselect_b32 s6, s6, 0xe0
	s_add_u32 s8, s8, s13
	s_addc_u32 s9, s9, s11
	v_readlane_b32 s15, v250, 14
	s_add_u32 s13, s15, s13
	v_readlane_b32 s15, v250, 15
	s_addc_u32 s11, s15, s11
	s_and_b32 s15, s10, 0xff
	s_mul_i32 s15, s15, 37
	s_lshr_b32 s15, s15, 8
	s_sub_i32 s16, s10, s15
	s_bfe_u32 s16, s16, 0x70001
	s_add_i32 s16, s16, s15
	s_bfe_u32 s15, s16, 0x60002
	v_lshl_or_b32 v2, s15, 6, v126
	s_mul_i32 s16, s15, 7
	v_mul_u32_u24_e32 v186, 0x1c00, v2
	v_lshl_add_u64 v[2:3], v[186:187], 2, s[8:9]
	s_sub_i32 s8, s10, s16
	s_and_b32 s8, s8, 0xff
	s_lshl_b32 s8, s8, 10
	s_add_i32 s8, s8, s18
	s_ashr_i32 s9, s8, 31
	v_lshl_add_u64 v[2:3], s[8:9], 2, v[2:3]
	v_mov_b32_e32 v131, v187
	v_lshl_add_u64 v[70:71], v[2:3], 0, v[130:131]
	s_movk_i32 s9, 0x7000
	v_add_co_u32_e32 v78, vcc, s9, v70
	s_mov_b32 s9, 0xe000
	s_nop 0
	v_addc_co_u32_e32 v79, vcc, 0, v71, vcc
	v_add_co_u32_e32 v86, vcc, s9, v70
	s_mov_b32 s9, 0x15000
	s_nop 0
	v_addc_co_u32_e32 v87, vcc, 0, v71, vcc
	v_add_co_u32_e32 v94, vcc, s9, v70
	s_mov_b32 s9, 0x1c000
	s_nop 0
	v_addc_co_u32_e32 v95, vcc, 0, v71, vcc
	v_add_co_u32_e32 v102, vcc, s9, v70
	s_mov_b32 s9, 0x23000
	s_nop 0
	v_addc_co_u32_e32 v103, vcc, 0, v71, vcc
	v_add_co_u32_e32 v110, vcc, s9, v70
	s_mov_b32 s9, 0x2a000
	s_nop 0
	v_addc_co_u32_e32 v111, vcc, 0, v71, vcc
	v_add_co_u32_e32 v118, vcc, s9, v70
	global_load_dwordx4 v[2:5], v[70:71], off nt
	global_load_dwordx4 v[6:9], v[78:79], off nt
	v_addc_co_u32_e32 v119, vcc, 0, v71, vcc
	global_load_dwordx4 v[10:13], v[86:87], off nt
; __device__ __forceinline__ unsigned cvt_pk_bf16(float lo, float hi) { f32x2_t v = {lo, hi}; bf16x2_t b = __builtin_convertvector(v, bf16x2_t); return __builtin_bit_cast(unsigned, b); }
; __device__ __forceinline__ void conv_span128(const float* W, int ldw, int K, bf16* WT, int rowmode, int kb, int n0, int lane) {
;     const int c = lane & 7, nn = lane >> 3;
;     const float* src = W + (size_t)(kb * 64 + 8 * c) * ldw + n0 + 4 * nn;
;     f32x4 v[4][8];
; #pragma unroll
;     for (int h = 0; h < 4; ++h)
; #pragma unroll
;         for (int i = 0; i < 8; ++i) v[h][i] = __builtin_nontemporal_load((const f32x4*)(src + 32 * h + (size_t)i * ldw));
; #pragma unroll
;     for (int h = 0; h < 4; ++h) {
;         const int n = n0 + 32 * h + 4 * nn; int r = n;
;         if (rowmode == 2) r = ((n >> 7) << 8) + (n & 127);
;         else if (rowmode == 3) r = ((n >> 7) << 8) + 128 + (n & 127);
;         bf16* d0 = WT + (size_t)r * K + kb * 64 + 8 * c;
; #pragma unroll
;         for (int j = 0; j < 4; ++j) { u32x4 o; o.x = cvt_pk_bf16(v[h][0][j], v[h][1][j]); o.y = cvt_pk_bf16(v[h][2][j], v[h][3][j]); o.z = cvt_pk_bf16(v[h][4][j], v[h][5][j]); o.w = cvt_pk_bf16(v[h][6][j], v[h][7][j]);
;             *(u32x4*)(d0 + (size_t)j * K) = o; }
;     }
;     ...
;         const int p = (int)(cur & 0x7FFFFFFFu);
;         if ((cur >> 31) == 0u) { const int e = p / 448, w3 = (p / 224) & 1, q = p % 224;
;             conv_span128((w3 ? m3 : m1) + (size_t)e * D * FFE, FFE, D, mup + (size_t)e * 2 * FFE * D, 2 + w3, q / 7, (q % 7) * 1024 + wave * 128, lane); }
	global_load_dwordx4 v[14:17], v[94:95], off nt
	global_load_dwordx4 v[18:21], v[102:103], off nt
	global_load_dwordx4 v[22:25], v[110:111], off nt
	global_load_dwordx4 v[26:29], v[118:119], off nt
	s_mov_b32 s9, 0x31000
	v_add_co_u32_e32 v134, vcc, s9, v70
	s_lshl_b32 s9, s15, 7
	s_nop 0
	v_addc_co_u32_e32 v135, vcc, 0, v71, vcc
	global_load_dwordx4 v[30:33], v[134:135], off nt
	global_load_dwordx4 v[34:37], v[70:71], off offset:128 nt
	global_load_dwordx4 v[38:41], v[78:79], off offset:128 nt
	global_load_dwordx4 v[42:45], v[86:87], off offset:128 nt
	global_load_dwordx4 v[46:49], v[94:95], off offset:128 nt
	global_load_dwordx4 v[50:53], v[102:103], off offset:128 nt
	global_load_dwordx4 v[54:57], v[110:111], off offset:128 nt
	global_load_dwordx4 v[58:61], v[118:119], off offset:128 nt
	global_load_dwordx4 v[62:65], v[134:135], off offset:128 nt
	global_load_dwordx4 v[66:69], v[70:71], off offset:256 nt
	s_nop 0
	global_load_dwordx4 v[70:73], v[70:71], off offset:384 nt
	s_nop 0
	global_load_dwordx4 v[74:77], v[78:79], off offset:256 nt
	s_nop 0
	global_load_dwordx4 v[78:81], v[78:79], off offset:384 nt
	s_nop 0
	global_load_dwordx4 v[82:85], v[86:87], off offset:256 nt
	s_nop 0
	global_load_dwordx4 v[86:89], v[86:87], off offset:384 nt
	s_nop 0
	global_load_dwordx4 v[90:93], v[94:95], off offset:256 nt
	s_nop 0
	global_load_dwordx4 v[94:97], v[94:95], off offset:384 nt
	s_nop 0
	global_load_dwordx4 v[98:101], v[102:103], off offset:256 nt
	s_nop 0
	global_load_dwordx4 v[102:105], v[102:103], off offset:384 nt
	s_nop 0
	global_load_dwordx4 v[106:109], v[110:111], off offset:256 nt
	s_nop 0
	global_load_dwordx4 v[110:113], v[110:111], off offset:384 nt
	s_nop 0
	global_load_dwordx4 v[114:117], v[118:119], off offset:256 nt
	s_nop 0
	global_load_dwordx4 v[118:121], v[118:119], off offset:384 nt
	s_nop 0
	global_load_dwordx4 v[122:125], v[134:135], off offset:256 nt
	s_nop 0
	global_load_dwordx4 v[134:137], v[134:135], off offset:384 nt
	s_add_u32 s10, s13, s9
	s_addc_u32 s11, s11, 0
	s_lshl_b32 s8, s8, 1
	v_lshl_or_b32 v131, s12, 7, v128
	v_or_b32_e32 v138, s8, v131
	v_mov_b32_e32 v133, v187
	v_ashrrev_i32_e32 v139, 31, v138
	v_lshl_add_u64 v[142:143], s[10:11], 0, v[132:133]
	v_lshlrev_b64 v[138:139], 12, v[138:139]
	v_lshl_add_u64 v[144:145], v[142:143], 0, v[138:139]
	s_movk_i32 s9, 0x2000
	s_movk_i32 s10, 0x3000
	v_readlane_b32 s41, v255, 8
	v_readlane_b32 s42, v255, 9
	v_readlane_b32 s43, v255, 10
	s_waitcnt vmcnt(30)
	v_cvt_pk_bf16_f32 v138, v2, v6
	v_add_co_u32_e32 v2, vcc, s9, v144
	s_waitcnt vmcnt(28)
	v_cvt_pk_bf16_f32 v139, v10, v14
	s_waitcnt vmcnt(26)
	v_cvt_pk_bf16_f32 v140, v18, v22
	s_waitcnt vmcnt(24)
	v_cvt_pk_bf16_f32 v141, v26, v30
	global_store_dwordx4 v[144:145], v[138:141], off
	s_nop 1
	v_cvt_pk_bf16_f32 v138, v3, v7
	v_cvt_pk_bf16_f32 v139, v11, v15
	v_cvt_pk_bf16_f32 v140, v19, v23
	v_cvt_pk_bf16_f32 v141, v27, v31
	v_addc_co_u32_e32 v3, vcc, 0, v145, vcc
	global_store_dwordx4 v[2:3], v[138:141], off offset:-4096
	v_add_co_u32_e32 v6, vcc, s10, v144
	s_nop 0
	v_cvt_pk_bf16_f32 v138, v4, v8
	v_cvt_pk_bf16_f32 v139, v12, v16
	v_cvt_pk_bf16_f32 v140, v20, v24
	v_cvt_pk_bf16_f32 v141, v28, v32
	global_store_dwordx4 v[2:3], v[138:141], off
	v_cvt_pk_bf16_f32 v2, v5, v9
	v_cvt_pk_bf16_f32 v3, v13, v17
	v_cvt_pk_bf16_f32 v4, v21, v25
	v_cvt_pk_bf16_f32 v5, v29, v33
	v_addc_co_u32_e32 v7, vcc, 0, v145, vcc
	global_store_dwordx4 v[6:7], v[2:5], off
	s_nop 1
	v_or_b32_e32 v2, s14, v128
	v_or_b32_e32 v2, s8, v2
	v_ashrrev_i32_e32 v3, 31, v2
	v_lshlrev_b64 v[2:3], 12, v[2:3]
	v_lshl_add_u64 v[6:7], v[142:143], 0, v[2:3]
	s_waitcnt vmcnt(26)
	v_cvt_pk_bf16_f32 v2, v34, v38
	s_waitcnt vmcnt(24)
	v_cvt_pk_bf16_f32 v3, v42, v46
	s_waitcnt vmcnt(22)
	v_cvt_pk_bf16_f32 v4, v50, v54
	s_waitcnt vmcnt(20)
	v_cvt_pk_bf16_f32 v5, v58, v62
	v_add_co_u32_e32 v8, vcc, s9, v6
	global_store_dwordx4 v[6:7], v[2:5], off
	s_nop 0
	v_addc_co_u32_e32 v9, vcc, 0, v7, vcc
	v_cvt_pk_bf16_f32 v2, v35, v39
	v_cvt_pk_bf16_f32 v3, v43, v47
	v_cvt_pk_bf16_f32 v4, v51, v55
	v_cvt_pk_bf16_f32 v5, v59, v63
	global_store_dwordx4 v[8:9], v[2:5], off offset:-4096
	v_add_co_u32_e32 v6, vcc, s10, v6
	s_nop 0
	v_cvt_pk_bf16_f32 v2, v36, v40
	v_cvt_pk_bf16_f32 v3, v44, v48
	v_cvt_pk_bf16_f32 v4, v52, v56
	v_cvt_pk_bf16_f32 v5, v60, v64
	global_store_dwordx4 v[8:9], v[2:5], off
	v_addc_co_u32_e32 v7, vcc, 0, v7, vcc
	s_nop 0
	v_cvt_pk_bf16_f32 v2, v37, v41
	v_cvt_pk_bf16_f32 v3, v45, v49
	v_cvt_pk_bf16_f32 v4, v53, v57
	v_cvt_pk_bf16_f32 v5, v61, v65
	global_store_dwordx4 v[6:7], v[2:5], off
	s_nop 1
	v_or_b32_e32 v2, s7, v128
	v_or_b32_e32 v2, s8, v2
	v_ashrrev_i32_e32 v3, 31, v2
	v_lshlrev_b64 v[2:3], 12, v[2:3]
	v_lshl_add_u64 v[6:7], v[142:143], 0, v[2:3]
	s_waitcnt vmcnt(21)
	v_cvt_pk_bf16_f32 v2, v66, v74
	s_waitcnt vmcnt(17)
	v_cvt_pk_bf16_f32 v3, v82, v90
	s_waitcnt vmcnt(13)
	v_cvt_pk_bf16_f32 v4, v98, v106
	s_waitcnt vmcnt(9)
	v_cvt_pk_bf16_f32 v5, v114, v122
	v_add_co_u32_e32 v8, vcc, s9, v6
	global_store_dwordx4 v[6:7], v[2:5], off
	s_nop 0
	v_addc_co_u32_e32 v9, vcc, 0, v7, vcc
	v_cvt_pk_bf16_f32 v2, v67, v75
	v_cvt_pk_bf16_f32 v3, v83, v91
	v_cvt_pk_bf16_f32 v4, v99, v107
	v_cvt_pk_bf16_f32 v5, v115, v123
	global_store_dwordx4 v[8:9], v[2:5], off offset:-4096
	v_add_co_u32_e32 v6, vcc, s10, v6
	s_nop 0
	v_cvt_pk_bf16_f32 v2, v68, v76
	v_cvt_pk_bf16_f32 v3, v84, v92
	v_cvt_pk_bf16_f32 v4, v100, v108
	v_cvt_pk_bf16_f32 v5, v116, v124
	global_store_dwordx4 v[8:9], v[2:5], off
	v_addc_co_u32_e32 v7, vcc, 0, v7, vcc
	s_nop 0
	v_cvt_pk_bf16_f32 v2, v69, v77
	v_cvt_pk_bf16_f32 v3, v85, v93
	v_cvt_pk_bf16_f32 v4, v101, v109
	v_cvt_pk_bf16_f32 v5, v117, v125
	global_store_dwordx4 v[6:7], v[2:5], off
	s_nop 1
	v_or_b32_e32 v2, s6, v128
	v_or_b32_e32 v2, s8, v2
	v_ashrrev_i32_e32 v3, 31, v2
	v_lshlrev_b64 v[2:3], 12, v[2:3]
	v_lshl_add_u64 v[6:7], v[142:143], 0, v[2:3]
	v_cvt_pk_bf16_f32 v2, v70, v78
	v_cvt_pk_bf16_f32 v3, v86, v94
	v_cvt_pk_bf16_f32 v4, v102, v110
	s_waitcnt vmcnt(12)
	v_cvt_pk_bf16_f32 v5, v118, v134
	v_add_co_u32_e32 v8, vcc, s9, v6
	global_store_dwordx4 v[6:7], v[2:5], off
	s_nop 0
	v_addc_co_u32_e32 v9, vcc, 0, v7, vcc
	v_cvt_pk_bf16_f32 v2, v71, v79
	v_cvt_pk_bf16_f32 v3, v87, v95
	v_cvt_pk_bf16_f32 v4, v103, v111
	v_cvt_pk_bf16_f32 v5, v119, v135
	global_store_dwordx4 v[8:9], v[2:5], off offset:-4096
	v_add_co_u32_e32 v6, vcc, 0x3000, v6
	s_nop 0
	v_cvt_pk_bf16_f32 v2, v72, v80
	v_cvt_pk_bf16_f32 v3, v88, v96
	v_cvt_pk_bf16_f32 v4, v104, v112
	v_cvt_pk_bf16_f32 v5, v120, v136
	global_store_dwordx4 v[8:9], v[2:5], off
	v_addc_co_u32_e32 v7, vcc, 0, v7, vcc
	s_nop 0
	v_cvt_pk_bf16_f32 v2, v73, v81
	v_cvt_pk_bf16_f32 v3, v89, v97
	v_cvt_pk_bf16_f32 v4, v105, v113
	v_cvt_pk_bf16_f32 v5, v121, v137
	global_store_dwordx4 v[6:7], v[2:5], off
	s_branch .LBB0_135

; __device__ __forceinline__ void signal_done(unsigned* p, int wave) { if (wave == 0 && __builtin_amdgcn_mbcnt_hi(~0u, __builtin_amdgcn_mbcnt_lo(~0u, 0u)) == 0u) xb_add(p, 1u); }
; __global__ void __launch_bounds__(NWAVES * 64, 2) trunk_fwd(Args args) {
;     ...
;         if (EN(4) && IN(pb + 3)) {
;             int tz = threadIdx.x; asm volatile("" : "+v"(tz)); const int lane = tz & 63; const int wave = __builtin_amdgcn_readfirstlane(tz >> 6); const int tid = tz; const int gw = bx * NWAVES + wave; (void)lane; (void)tid; (void)gw;
;             for (int L = bx; L < 512; L += G) { int bg, iq; if (L < 256) { bg = L >> 4; iq = 31 - (L & 15); } else { bg = (L - 256) >> 4; iq = (L - 256) & 15; }
;                 nsa::unit(lds, Zb, KCT, KCT + (size_t)16 * 128 * 64, OA, bg >> 2, bg & 3, iq, tz); }
;             __syncthreads();
;             signal_done(ctl + CW_DONE(6 + layer), wave);
.LBB0_393:
	s_andn2_b64 vcc, exec, s[0:1]
	s_cbranch_vccnz .LBB0_582
	v_readlane_b32 s0, v252, 2
	v_readlane_b32 s1, v252, 3
	v_mov_b32_e32 v123, v0
	s_andn2_b64 vcc, exec, s[0:1]
	v_readlane_b32 s0, v254, 40
	s_mov_b32 s21, s0
	v_readfirstlane_b32 s20, v123
	s_cmpk_lt_u32 s20, 0x100
	s_cbranch_scc1 .Lnsa_prio_skip
	s_setprio 1
.Lnsa_prio_skip:
	v_readlane_b32 s1, v254, 41
	s_cbranch_vccz .LBB0_412
.LBB0_395:
	s_setprio 0
	v_readlane_b32 s0, v255, 16
	v_readlane_b32 s1, v255, 17
	s_lshl_b32 s28, s0, 5
	s_lshl_b64 s[0:1], s[28:29], 2
	v_readlane_b32 s4, v250, 6
	v_readlane_b32 s5, v250, 7
	s_add_u32 s0, s4, s0
	s_addc_u32 s1, s5, s1
	s_add_u32 s4, s0, 0x8400
	s_addc_u32 s5, s1, 0
	s_cmp_gt_u32 s20, 63
	s_waitcnt vmcnt(0)
	s_barrier
	s_cbranch_scc1 .LBB0_400
	v_cmp_eq_u32_e32 vcc, 0, v228
	s_and_saveexec_b64 s[0:1], vcc
	s_cbranch_execz .LBB0_399
	s_mov_b64 s[6:7], exec
	v_mbcnt_lo_u32_b32 v1, s6, 0
	v_mbcnt_hi_u32_b32 v1, s7, v1
	v_cmp_eq_u32_e32 vcc, 0, v1
	s_and_b64 s[8:9], exec, vcc
	s_mov_b64 exec, s[8:9]
	s_cbranch_execz .LBB0_399
	s_bcnt1_i32_b64 s6, s[6:7]
	v_mov_b32_e32 v1, s6
	global_atomic_add v187, v1, s[4:5]
